# moe_combine loop: removed two loop-top vmcnt waits that only drained the previous iteration's output stores (record registers already complete on both paths)
# baseline (speedup 1.0000x reference)
.LBB0_641:
	s_add_i32 s4, 0, 0x20200
	v_lshlrev_b32_e32 v0, 2, v6
	v_add_u32_e32 v0, s4, v0
	ds_read_b32 v0, v0
	s_add_i32 s36, s40, s88
	s_min_i32 s42, s36, 0x3fff
	s_ashr_i32 s43, s42, 31
	v_mov_b64_e32 v[44:45], v[12:13]
	s_waitcnt lgkmcnt(0)
	v_lshlrev_b32_e32 v0, 8, v0
	v_add_u32_e32 v2, v0, v2
	v_lshlrev_b32_e32 v0, 2, v7
	v_add_u32_e32 v0, s4, v0
	ds_read_b32 v0, v0
	s_lshl_b64 s[42:43], s[42:43], 11
	v_mov_b64_e32 v[42:43], v[10:11]
	v_lshl_add_u64 v[10:11], v[52:53], 0, s[42:43]
	s_add_i32 s37, s90, s40
	s_waitcnt lgkmcnt(0)
	v_lshlrev_b32_e32 v0, 8, v0
	v_add_u32_e32 v6, v0, v3
	v_lshlrev_b32_e32 v0, 2, v8
	v_add_u32_e32 v0, s4, v0
	ds_read_b32 v0, v0
	v_ashrrev_i32_e32 v3, 31, v2
	v_lshlrev_b64 v[2:3], 10, v[2:3]
	v_lshl_add_u64 v[2:3], v[54:55], 0, v[2:3]
	v_ashrrev_i32_e32 v7, 31, v6
	s_waitcnt lgkmcnt(0)
	v_lshlrev_b32_e32 v0, 8, v0
	v_add_u32_e32 v4, v0, v4
	v_lshlrev_b32_e32 v0, 2, v9
	v_add_u32_e32 v0, s4, v0
	ds_read_b32 v0, v0
	global_load_dwordx4 v[34:37], v[10:11], off nt
	global_load_dwordx4 v[30:33], v[10:11], off offset:1024 nt
	global_load_dwordx2 v[74:75], v[2:3], off nt
	global_load_dwordx2 v[72:73], v[2:3], off offset:512 nt
	v_lshlrev_b64 v[2:3], 10, v[6:7]
	v_lshl_add_u64 v[2:3], v[54:55], 0, v[2:3]
	s_waitcnt lgkmcnt(0)
	v_lshlrev_b32_e32 v0, 8, v0
	v_add_u32_e32 v8, v0, v5
	v_ashrrev_i32_e32 v5, 31, v4
	s_min_i32 s42, s37, 0x3fff
	global_load_dwordx2 v[70:71], v[2:3], off nt
	global_load_dwordx2 v[68:69], v[2:3], off offset:512 nt
	v_lshlrev_b64 v[2:3], 10, v[4:5]
	s_ashr_i32 s43, s42, 31
	v_lshl_add_u64 v[2:3], v[54:55], 0, v[2:3]
	v_ashrrev_i32_e32 v9, 31, v8
	s_lshl_b64 s[42:43], s[42:43], 4
	global_load_dwordx2 v[66:67], v[2:3], off nt
	global_load_dwordx2 v[64:65], v[2:3], off offset:512 nt
	v_lshlrev_b64 v[2:3], 10, v[8:9]
	s_add_u32 s44, s5, s42
	s_waitcnt vmcnt(8)
	v_mov_b64_e32 v[48:49], v[20:21]
	v_lshl_add_u64 v[2:3], v[54:55], 0, v[2:3]
	s_addc_u32 s45, s6, s43
	v_mov_b64_e32 v[46:47], v[18:19]
	global_load_dwordx2 v[62:63], v[2:3], off nt
	global_load_dwordx2 v[60:61], v[2:3], off offset:512 nt
	global_load_dwordx4 v[18:21], v1, s[44:45]
	s_add_u32 s44, s14, s42
	s_addc_u32 s45, s15, s43
	v_lshlrev_b32_e32 v0, 2, v49
	s_add_u32 s42, s16, s42
	v_add_u32_e32 v0, s4, v0
	v_mov_b64_e32 v[40:41], v[16:17]
	s_addc_u32 s43, s17, s43
	s_add_i32 s37, s46, s40
	ds_read_b32 v0, v0
	v_mov_b64_e32 v[38:39], v[14:15]
	global_load_dwordx4 v[10:13], v1, s[44:45]
	global_load_dwordx4 v[14:17], v1, s[42:43]
	s_min_i32 s42, s37, 0x3fff
	s_ashr_i32 s43, s42, 31
	s_lshl_b64 s[42:43], s[42:43], 4
	s_add_u32 s44, s5, s42
	s_addc_u32 s45, s6, s43
	s_waitcnt lgkmcnt(0)
	v_lshlrev_b32_e32 v0, 8, v0
	global_load_dwordx4 v[6:9], v1, s[44:45]
	s_add_u32 s44, s14, s42
	v_add_u32_e32 v76, v0, v45
	s_addc_u32 s45, s15, s43
	v_ashrrev_i32_e32 v77, 31, v76
	s_add_u32 s42, s16, s42
	v_lshlrev_b64 v[76:77], 10, v[76:77]
	v_lshlrev_b32_e32 v0, 2, v48
	s_addc_u32 s43, s17, s43
	v_lshl_add_u64 v[78:79], v[54:55], 0, v[76:77]
	v_add_u32_e32 v0, s4, v0
	global_load_dwordx4 v[2:5], v1, s[44:45]
	global_load_dwordx4 v[26:29], v1, s[42:43]
	global_load_dwordx2 v[76:77], v[78:79], off offset:512 nt
	s_nop 0
	global_load_dwordx2 v[78:79], v[78:79], off nt
	ds_read_b32 v0, v0
	s_ashr_i32 s41, s40, 31
	s_lshl_b64 s[42:43], s[40:41], 11
	s_mov_b64 s[44:45], -1
	s_waitcnt lgkmcnt(0)
	v_lshlrev_b32_e32 v0, 8, v0
	v_add_u32_e32 v44, v0, v44
	v_ashrrev_i32_e32 v45, 31, v44
	v_lshlrev_b64 v[44:45], 10, v[44:45]
	v_lshlrev_b32_e32 v0, 2, v47
	v_lshl_add_u64 v[44:45], v[54:55], 0, v[44:45]
	v_add_u32_e32 v0, s4, v0
	global_load_dwordx2 v[80:81], v[44:45], off offset:512 nt
	global_load_dwordx2 v[82:83], v[44:45], off nt
	ds_read_b32 v0, v0
	s_waitcnt lgkmcnt(0)
	v_lshlrev_b32_e32 v0, 8, v0
	v_add_u32_e32 v44, v0, v43
	v_ashrrev_i32_e32 v45, 31, v44
	v_lshlrev_b64 v[44:45], 10, v[44:45]
	v_lshlrev_b32_e32 v0, 2, v46
	v_lshl_add_u64 v[44:45], v[54:55], 0, v[44:45]
	v_add_u32_e32 v0, s4, v0
	global_load_dwordx2 v[84:85], v[44:45], off offset:512 nt
	global_load_dwordx2 v[86:87], v[44:45], off nt
	ds_read_b32 v0, v0
	v_lshl_add_u64 v[46:47], v[52:53], 0, s[42:43]
	s_waitcnt lgkmcnt(0)
	v_lshlrev_b32_e32 v0, 8, v0
	v_add_u32_e32 v42, v0, v42
	v_ashrrev_i32_e32 v43, 31, v42
	v_lshlrev_b64 v[42:43], 10, v[42:43]
	v_lshl_add_u64 v[42:43], v[54:55], 0, v[42:43]
	global_load_dwordx2 v[88:89], v[42:43], off offset:512 nt
	global_load_dwordx2 v[90:91], v[42:43], off nt
	s_nop 0
	global_load_dwordx4 v[42:45], v[46:47], off offset:1024 nt
	s_nop 0
	global_load_dwordx4 v[46:49], v[46:47], off nt
	v_mov_b32_e32 v0, v41
	s_waitcnt vmcnt(8)
	v_cvt_pk_f32_fp8_sdwa v[130:131], v78 src0_sel:WORD_1
	v_cvt_pk_f32_fp8_e32 v[132:133], v79
	v_cvt_pk_f32_fp8_sdwa v[134:135], v79 src0_sel:WORD_1
	s_waitcnt vmcnt(7)
	v_cvt_pk_f32_fp8_e32 v[122:123], v80
	s_waitcnt vmcnt(6)
	v_cvt_pk_f32_fp8_e32 v[116:117], v82
	v_cvt_pk_f32_fp8_sdwa v[124:125], v80 src0_sel:WORD_1
	v_cvt_pk_f32_fp8_e32 v[126:127], v81
	v_cvt_pk_f32_fp8_sdwa v[128:129], v81 src0_sel:WORD_1
	v_cvt_pk_f32_fp8_e32 v[80:81], v78
	v_cvt_pk_f32_fp8_sdwa v[118:119], v82 src0_sel:WORD_1
	v_cvt_pk_f32_fp8_e32 v[120:121], v83
	v_cvt_pk_f32_fp8_sdwa v[82:83], v83 src0_sel:WORD_1
	s_waitcnt vmcnt(5)
	v_cvt_pk_f32_fp8_e32 v[110:111], v84
	s_waitcnt vmcnt(4)
	v_cvt_pk_f32_fp8_e32 v[104:105], v86
	v_cvt_pk_f32_fp8_sdwa v[106:107], v86 src0_sel:WORD_1
	v_cvt_pk_f32_fp8_e32 v[108:109], v87
	v_cvt_pk_f32_fp8_sdwa v[86:87], v87 src0_sel:WORD_1
	v_cvt_pk_f32_fp8_sdwa v[112:113], v84 src0_sel:WORD_1
	v_cvt_pk_f32_fp8_e32 v[114:115], v85
	v_cvt_pk_f32_fp8_sdwa v[84:85], v85 src0_sel:WORD_1
	s_waitcnt vmcnt(3)
	v_cvt_pk_f32_fp8_e32 v[98:99], v88
	s_waitcnt vmcnt(2)
	v_cvt_pk_f32_fp8_e32 v[92:93], v90
	s_waitcnt vmcnt(0)
	v_lshlrev_b32_e32 v78, 16, v46
	v_and_b32_e32 v79, 0xffff0000, v46
	v_cvt_pk_f32_fp8_sdwa v[94:95], v90 src0_sel:WORD_1
	v_cvt_pk_f32_fp8_e32 v[96:97], v91
	v_cvt_pk_f32_fp8_sdwa v[90:91], v91 src0_sel:WORD_1
	v_pk_fma_f32 v[78:79], v[38:39], v[92:93], v[78:79] op_sel_hi:[0,1,1]
	v_pk_fma_f32 v[78:79], v[38:39], v[104:105], v[78:79] op_sel:[1,0,0]
	v_cvt_pk_f32_fp8_sdwa v[100:101], v88 src0_sel:WORD_1
	v_pk_fma_f32 v[78:79], v[40:41], v[116:117], v[78:79] op_sel_hi:[0,1,1]
	v_pk_fma_f32 v[78:79], v[0:1], v[80:81], v[78:79] op_sel_hi:[0,1,1]
	v_lshlrev_b32_e32 v80, 16, v48
	v_and_b32_e32 v81, 0xffff0000, v48
	v_lshlrev_b32_e32 v48, 16, v49
	v_and_b32_e32 v49, 0xffff0000, v49
	v_pk_fma_f32 v[48:49], v[38:39], v[90:91], v[48:49] op_sel_hi:[0,1,1]
	v_pk_fma_f32 v[48:49], v[38:39], v[86:87], v[48:49] op_sel:[1,0,0]
	v_cvt_pk_f32_fp8_sdwa v[86:87], v76 src0_sel:WORD_1
	v_pk_fma_f32 v[48:49], v[40:41], v[82:83], v[48:49] op_sel_hi:[0,1,1]
	v_cvt_pk_f32_fp8_e32 v[82:83], v76
	v_cvt_pk_f32_fp8_e32 v[90:91], v77
	v_cvt_pk_f32_fp8_sdwa v[92:93], v77 src0_sel:WORD_1
	v_lshlrev_b32_e32 v76, 16, v42
	v_and_b32_e32 v77, 0xffff0000, v42
	v_cvt_pk_f32_fp8_e32 v[102:103], v89
	v_cvt_pk_f32_fp8_sdwa v[88:89], v89 src0_sel:WORD_1
	v_pk_fma_f32 v[76:77], v[38:39], v[98:99], v[76:77] op_sel_hi:[0,1,1]
	v_lshlrev_b32_e32 v46, 16, v47
	v_and_b32_e32 v47, 0xffff0000, v47
	v_pk_fma_f32 v[76:77], v[38:39], v[110:111], v[76:77] op_sel:[1,0,0]
	v_pk_fma_f32 v[46:47], v[38:39], v[94:95], v[46:47] op_sel_hi:[0,1,1]
	v_pk_fma_f32 v[80:81], v[38:39], v[96:97], v[80:81] op_sel_hi:[0,1,1]
	v_pk_fma_f32 v[76:77], v[40:41], v[122:123], v[76:77] op_sel_hi:[0,1,1]
	v_lshlrev_b32_e32 v42, 16, v43
	v_and_b32_e32 v43, 0xffff0000, v43
	v_pk_fma_f32 v[46:47], v[38:39], v[106:107], v[46:47] op_sel:[1,0,0]
	v_pk_fma_f32 v[80:81], v[38:39], v[108:109], v[80:81] op_sel:[1,0,0]
	v_pk_fma_f32 v[76:77], v[0:1], v[82:83], v[76:77] op_sel_hi:[0,1,1]
	v_pk_fma_f32 v[42:43], v[38:39], v[100:101], v[42:43] op_sel_hi:[0,1,1]
	v_lshlrev_b32_e32 v82, 16, v44
	v_and_b32_e32 v83, 0xffff0000, v44
	v_lshlrev_b32_e32 v44, 16, v45
	v_and_b32_e32 v45, 0xffff0000, v45
	v_pk_fma_f32 v[46:47], v[40:41], v[118:119], v[46:47] op_sel_hi:[0,1,1]
	v_pk_fma_f32 v[80:81], v[40:41], v[120:121], v[80:81] op_sel_hi:[0,1,1]
	v_pk_fma_f32 v[42:43], v[38:39], v[112:113], v[42:43] op_sel:[1,0,0]
	v_pk_fma_f32 v[82:83], v[38:39], v[102:103], v[82:83] op_sel_hi:[0,1,1]
	v_pk_fma_f32 v[44:45], v[38:39], v[88:89], v[44:45] op_sel_hi:[0,1,1]
	v_pk_fma_f32 v[46:47], v[0:1], v[130:131], v[46:47] op_sel_hi:[0,1,1]
	v_pk_fma_f32 v[80:81], v[0:1], v[132:133], v[80:81] op_sel_hi:[0,1,1]
	v_pk_fma_f32 v[48:49], v[0:1], v[134:135], v[48:49] op_sel_hi:[0,1,1]
	v_pk_fma_f32 v[42:43], v[40:41], v[124:125], v[42:43] op_sel_hi:[0,1,1]
	v_pk_fma_f32 v[82:83], v[38:39], v[114:115], v[82:83] op_sel:[1,0,0]
	v_pk_fma_f32 v[38:39], v[38:39], v[84:85], v[44:45] op_sel:[1,0,0]
	v_pk_fma_f32 v[42:43], v[0:1], v[86:87], v[42:43] op_sel_hi:[0,1,1]
	v_pk_fma_f32 v[82:83], v[40:41], v[126:127], v[82:83] op_sel_hi:[0,1,1]
	v_pk_fma_f32 v[38:39], v[40:41], v[128:129], v[38:39] op_sel_hi:[0,1,1]
	v_pk_mul_f32 v[40:41], v[78:79], v[78:79]
	v_pk_mul_f32 v[44:45], v[46:47], v[46:47]
	v_pk_mul_f32 v[84:85], v[80:81], v[80:81]
	v_pk_mul_f32 v[86:87], v[48:49], v[48:49]
	v_pk_fma_f32 v[82:83], v[0:1], v[90:91], v[82:83] op_sel_hi:[0,1,1]
	v_pk_fma_f32 v[38:39], v[0:1], v[92:93], v[38:39] op_sel_hi:[0,1,1]
	v_add_f32_e32 v0, v86, v87
	v_add_f32_e32 v84, v84, v85
	v_add_f32_e32 v44, v44, v45
	v_add_f32_e32 v40, v40, v41
	v_pk_mul_f32 v[88:89], v[76:77], v[76:77]
	v_pk_mul_f32 v[90:91], v[42:43], v[42:43]
	v_add_f32_e32 v0, v84, v0
	v_add_f32_e32 v40, v40, v44
	v_add_f32_e32 v0, v40, v0
	v_add_f32_e32 v40, v90, v91
	v_add_f32_e32 v41, v88, v89
	v_pk_mul_f32 v[92:93], v[82:83], v[82:83]
	v_pk_mul_f32 v[94:95], v[38:39], v[38:39]
	v_add_f32_e32 v40, v41, v40
	v_add_f32_e32 v0, v0, v40
	v_add_f32_e32 v40, v94, v95
	v_add_f32_e32 v41, v92, v93
	v_add_f32_e32 v40, v41, v40
	v_add_f32_e32 v0, v0, v40
	s_nop 1
	v_add_f32_dpp v0, v0, v0 quad_perm:[1,0,3,2] row_mask:0xf bank_mask:0xf bound_ctrl:1
	s_nop 1
	v_add_f32_dpp v0, v0, v0 quad_perm:[2,3,0,1] row_mask:0xf bank_mask:0xf bound_ctrl:1
	s_nop 1
	v_add_f32_dpp v0, v0, v0 row_half_mirror row_mask:0xf bank_mask:0xf bound_ctrl:1
	s_nop 1
	v_add_f32_dpp v0, v0, v0 row_mirror row_mask:0xf bank_mask:0xf bound_ctrl:1
	v_mov_b32_e32 v40, v0
	s_nop 1
	v_permlane16_swap_b32_e32 v0, v40
	v_add_f32_e32 v0, v0, v40
	v_mov_b32_e32 v40, v0
	s_nop 1
	v_permlane32_swap_b32_e32 v0, v40
	v_add_f32_e32 v0, v0, v40
	v_fmamk_f32 v0, v0, 0x3a800000, v190
	v_cmp_gt_f32_e32 vcc, s96, v0
	v_mul_f32_e32 v40, 0x4b800000, v0
	s_nop 0
	v_cndmask_b32_e32 v0, v0, v40, vcc
	v_rsq_f32_e32 v0, v0
	s_nop 0
	v_mul_f32_e32 v40, 0x45800000, v0
	v_cndmask_b32_e32 v0, v0, v40, vcc
	s_and_b64 vcc, exec, s[30:31]
	s_cbranch_vccz .LBB0_646
	v_lshl_add_u64 v[40:41], v[56:57], 0, s[42:43]
	v_cvt_pk_bf16_f32 v84, v78, v79
	v_cvt_pk_bf16_f32 v85, v46, v47
	v_cvt_pk_bf16_f32 v86, v80, v81
	v_cvt_pk_bf16_f32 v87, v48, v49
	v_cvt_pk_bf16_f32 v88, v76, v77
	v_cvt_pk_bf16_f32 v89, v42, v43
	v_cvt_pk_bf16_f32 v90, v82, v83
	v_cvt_pk_bf16_f32 v91, v38, v39
	global_store_dwordx4 v[40:41], v[84:87], off
	global_store_dwordx4 v[40:41], v[88:91], off offset:1024
	s_and_saveexec_b64 s[42:43], s[38:39]
	s_cbranch_execz .LBB0_644
	s_lshl_b64 s[44:45], s[40:41], 2
	s_add_u32 s44, s26, s44
	s_addc_u32 s45, s27, s45
	global_store_dword v226, v0, s[44:45]
